# v13 + diff attention dense K LDS image (128-B rows, chunk XOR swizzle): one K LDS-DMA per wave and tile instead of two (the baseline image moved every K row twice)
# speedup vs baseline: 1.0074x; 1.0000x over previous
; #define LAS __attribute__((address_space(3)))
; __device__ __forceinline__ int v_rd_base(int lane) { return ((lane & 3) << 3) | (((lane >> 2) & 3) << 6) | (((lane >> 4) & 1) << 5) | (((lane >> 5) & 1) << 8); }
; #define DMA_WAIT(last) do { if (last) asm volatile("s_waitcnt vmcnt(0)" ::: "memory"); else asm volatile("s_waitcnt vmcnt(%0)" :: "n"(NPW) : "memory"); } while (0)
; template <int DK, int DV, bool OFF, class QLoader> ...
;     ...
;   for (int i = 0; i < (DK == 64 ? 1 : KPW); ++i) { const int row = (wid * KPW + i) * 4 + (lane >> 4); int c = (lane & 15) ^ (row & 7); c = (c < DK / 8) ? c : (c & 7); koff[i] = (unsigned)((row * ldk) * 2 + c * 16); }
; #pragma unroll
;   for (int i = 0; i < 1; ++i) { const int sidx = (wid * VPW + i) * 2 + (lane >> 5), kg = sidx / ND, st = sidx % ND, kk = kg * 8 + ((lane & 31) >> 2);
;     const int k = (kk & ~0xC) | ((kk & 4) << 1) | ((kk & 8) >> 1), c = st * 32 + (lane & 3) * 8; voff[i] = (unsigned)((k * ldv + c) * 2); }
;   const int vb0 = (int)(uintptr_t)V_lds + v_rd_base(lane);
;   LAS unsigned* const ldsK = (LAS unsigned*)(LAS char*)K_lds + (wid * KPW) * 256; LAS unsigned* const ldsV = (LAS unsigned*)(LAS char*)V_lds + (wid * VPW) * 256;
;     ...
;   f32x16 pA0, pA1, pB0, pB1; bf16x8 pa0, pa1, pa2, pa3; const int NT = nkeys / KVBLK;
;   DMA_TILE(0, 0); DMA_TILE(1, 1); DMA_WAIT(false); __syncthreads(); if (2 < NT) DMA_TILE(2, 2);
;   qkt<DK>(pA0, pA1, K_lds, qr, r32, hi); partialSM<DK, OFF>(pA0, pA1, negMC);
.LBB0_838:
	s_and_b64 s[16:17], s[14:15], exec
	s_cselect_b32 s76, s12, s2
	s_ashr_i32 s2, s76, 4
	s_and_b32 s22, s76, 15
	s_mul_i32 s78, s76, 0x88000
	s_mul_hi_i32 s77, s76, 0x88000
	s_add_u32 s16, s65, s78
	s_addc_u32 s17, s66, s77
	s_lshl_b32 s4, s2, 8
	s_add_i32 s23, s4, 0x8000
	s_mul_i32 s80, s23, 0x1800
	s_mul_hi_i32 s79, s23, 0x1800
	s_add_u32 s4, s67, s80
	s_addc_u32 s12, s68, s79
	s_lshl_b32 s13, s76, 7
	s_and_b32 s13, s13, 0x700
	s_add_u32 s4, s4, s13
	s_addc_u32 s12, s12, 0
	s_add_u32 s18, s4, 0x1000
	s_addc_u32 s19, s12, 0
	s_lshl_b32 s12, s2, 12
	s_mul_i32 s2, s2, 0x1800000
	s_mul_hi_i32 s4, s12, 0x1800
	s_add_u32 s24, s67, s2
	s_addc_u32 s25, s68, s4
	s_add_u32 s13, s24, s13
	s_addc_u32 s24, s25, 0
	s_add_u32 s74, s13, 0x1000
	s_addc_u32 s75, s24, 0
	s_lshl_b32 s5, s5, 8
	s_or_b32 s5, s12, s5
	s_and_b64 s[12:13], s[14:15], exec
	s_cselect_b32 s12, s5, s23
	s_ashr_i32 s13, s12, 31
	s_lshl_b64 s[12:13], s[12:13], 12
	s_add_u32 s5, s69, s12
	s_addc_u32 s13, s70, s13
	s_lshl_b32 s12, s22, 8
	s_add_u32 s12, s5, s12
	s_addc_u32 s13, s13, 0
	s_andn2_b64 vcc, exec, s[34:35]
	s_mov_b64 s[22:23], -1
	s_cbranch_vccnz .LBB0_882
	v_mov_b32_e32 v25, v159
	v_mov_b32_e32 v33, v1
	v_readfirstlane_b32 s23, v25
	s_ashr_i32 s26, s23, 6
	v_and_b32_e32 v10, 31, v25
	s_lshl_b32 s22, s26, 5
	v_or_b32_e32 v2, s22, v10
	v_ashrrev_i32_e32 v3, 31, v2
	v_bfe_u32 v4, v25, 5, 1
	v_lshlrev_b64 v[2:3], 7, v[2:3]
	v_lshl_add_u64 v[2:3], s[20:21], 0, v[2:3]
	v_lshlrev_b32_e32 v32, 4, v4
	v_lshl_add_u64 v[2:3], v[2:3], 0, v[32:33]
	global_load_dwordx4 v[114:117], v[2:3], off
	global_load_dwordx4 v[118:121], v[2:3], off offset:32
	global_load_dwordx4 v[122:125], v[2:3], off offset:64
	global_load_dwordx4 v[126:129], v[2:3], off offset:96
	v_bfe_u32 v0, v25, 4, 2
	s_bfe_i32 s24, s26, 0x1001d
	v_and_b32_e32 v2, 15, v25
	v_bitop3_b32 v3, v0, v25, 15 bitop3:0x78
	v_lshl_or_b32 v20, s26, 2, v4
	s_lshr_b32 s24, s24, 30
	v_lshlrev_b32_e32 v3, 4, v3
	v_cmp_gt_u32_e32 vcc, 8, v2
	v_add_u32_e32 v2, s24, v20
	v_and_b32_e32 v5, 0x70, v3
	v_ashrrev_i32_e32 v21, 2, v2
	v_cndmask_b32_e32 v19, v5, v3, vcc
	v_lshlrev_b32_e32 v4, 3, v21
	v_bfe_u32 v5, v25, 2, 3
	v_bitop3_b32 v22, v4, -13, v5 bitop3:0xc8
	v_lshrrev_b32_e32 v4, 1, v25
	s_lshl_b32 s5, s26, 10
	v_lshlrev_b32_e32 v18, 7, v0
	v_and_b32_e32 v23, 8, v4
	v_and_b32_e32 v26, 4, v2
	v_or_b32_e32 v0, s5, v18
	v_and_b32_e32 v3, 0x3fffffc, v2
	v_or3_b32 v2, v23, v22, v26
	s_movk_i32 s24, 0xc00
	v_add_u32_e32 v0, v0, v19
	v_lshlrev_b32_e32 v4, 3, v25
	v_mul_lo_u32 v2, v2, s24
	s_add_i32 s27, 0, 0x10000
	s_lshl_b32 s24, s26, 11
	v_sub_u32_e32 v3, v20, v3
	v_and_b32_e32 v24, 24, v4
	s_add_i32 s81, s27, s5
	v_bfe_u32 v150, v25, 3, 3
	v_and_b32_e32 v0, 7, v25
	v_xor_b32_e32 v0, v0, v150
	v_lshlrev_b32_e32 v0, 4, v0
	v_lshl_or_b32 v0, v150, 7, v0
	v_or_b32_e32 v0, s5, v0
	v_mov_b32_e32 v151, v1
	v_lshl_or_b32 v3, v3, 5, v24
	s_add_i32 s82, s24, 0
	s_mov_b32 m0, s81
	v_lshl_add_u64 v[4:5], s[16:17], 0, v[150:151]
	s_mov_b64 s[24:25], 0x200
	s_add_i32 s83, s81, 0x400
	v_add_lshl_u32 v148, v3, v2, 1
	global_load_lds_dwordx4 v0, s[16:17]
	v_lshl_add_u64 v[6:7], v[4:5], 0, s[24:25]
	s_mov_b32 m0, s83
	v_mov_b32_e32 v149, v1
	v_lshl_add_u64 v[6:7], s[18:19], 0, v[148:149]
	s_mov_b32 m0, s82
	s_add_i32 s84, s82, 0x400
	v_lshl_add_u64 v[2:3], s[16:17], 0, v[0:1]
	global_load_lds_dwordx4 v148, s[18:19]
	v_lshl_add_u64 v[8:9], v[6:7], 0, s[10:11]
	s_mov_b32 m0, s84
	s_mov_b64 s[24:25], 0x2000
	s_add_i32 s85, s81, 0x4000
	global_load_lds_dwordx4 v[8:9], off
	v_lshl_add_u64 v[8:9], v[2:3], 0, s[24:25]
	s_mov_b32 m0, s85
	s_mov_b64 s[24:25], 0x2200
	s_add_i32 s86, s81, 0x4400
	global_load_lds_dwordx4 v[8:9], off
	v_lshl_add_u64 v[8:9], v[4:5], 0, s[24:25]
	s_mov_b32 m0, s86
	s_mov_b64 s[24:25], 0x60000
	s_add_i32 s87, s82, 0x4000
	v_lshl_add_u64 v[8:9], v[6:7], 0, s[24:25]
	s_mov_b32 m0, s87
	s_mov_b64 s[24:25], 0x60080
	s_add_i32 s88, s82, 0x4400
	global_load_lds_dwordx4 v[8:9], off
	v_lshl_add_u64 v[8:9], v[6:7], 0, s[24:25]
	s_mov_b32 m0, s88
	s_mov_b64 s[24:25], 0x4000
	s_add_i32 s89, s81, 0x8000
	global_load_lds_dwordx4 v[8:9], off
	v_lshl_add_u64 v[2:3], v[2:3], 0, s[24:25]
	s_mov_b32 m0, s89
	s_mov_b64 s[24:25], 0x4200
	s_add_i32 s90, s81, 0x8400
	s_waitcnt vmcnt(4)
	s_waitcnt vmcnt(0) lgkmcnt(0)
	s_barrier
	global_load_lds_dwordx4 v[2:3], off
	v_lshl_add_u64 v[2:3], v[4:5], 0, s[24:25]
	s_mov_b32 m0, s90
	s_mov_b64 s[24:25], 0xc0000
	s_add_i32 s91, s82, 0x8000
	v_lshl_add_u64 v[2:3], v[6:7], 0, s[24:25]
	s_mov_b32 m0, s91
	s_mov_b64 s[24:25], 0xc0080
	s_add_i32 s92, s82, 0x8400
	global_load_lds_dwordx4 v[2:3], off
	v_lshl_add_u64 v[2:3], v[6:7], 0, s[24:25]
	s_mov_b32 m0, s92
	v_lshlrev_b32_e32 v27, 7, v10
	global_load_lds_dwordx4 v[2:3], off
	v_lshlrev_b32_e32 v2, 4, v25
	v_and_b32_e32 v33, 0x70, v2
	v_bitop3_b32 v161, v32, v27, v33 bitop3:0xde
	v_add_u32_e32 v162, s27, v161
	ds_read_b128 v[2:5], v162
	ds_read_b128 v[28:31], v162 offset:4096
	s_waitcnt lgkmcnt(0)
	v_mfma_f32_32x32x16_bf16 v[66:81], v[28:31], v[114:117], 0
	v_or_b32_e32 v28, 32, v32
	v_bitop3_b32 v163, v28, v27, v33 bitop3:0xde
	v_add_u32_e32 v164, s27, v163
	ds_read_b128 v[28:31], v164
	s_cmp_lt_i32 s26, 4
	v_mfma_f32_32x32x16_bf16 v[2:17], v[2:5], v[114:117], 0
	s_waitcnt lgkmcnt(0)
	v_mfma_f32_32x32x16_bf16 v[2:17], v[28:31], v[118:121], v[2:17]
	ds_read_b128 v[28:31], v164 offset:4096
	s_waitcnt lgkmcnt(0)
	v_mfma_f32_32x32x16_bf16 v[66:81], v[28:31], v[118:121], v[66:81]
	v_or_b32_e32 v28, 64, v32
	v_bitop3_b32 v165, v28, v27, v33 bitop3:0xde
	v_add_u32_e32 v166, s27, v165
	ds_read_b128 v[28:31], v166
	s_waitcnt lgkmcnt(0)
	v_mfma_f32_32x32x16_bf16 v[2:17], v[28:31], v[122:125], v[2:17]
	ds_read_b128 v[28:31], v166 offset:4096
	s_waitcnt lgkmcnt(0)
	v_mfma_f32_32x32x16_bf16 v[66:81], v[28:31], v[122:125], v[66:81]
	v_or_b32_e32 v28, 0x60, v32
	v_bitop3_b32 v167, v28, v27, v33 bitop3:0xde
	v_add_u32_e32 v168, s27, v167
	ds_read_b128 v[28:31], v168
	s_waitcnt lgkmcnt(0)
	v_mfma_f32_32x32x16_bf16 v[2:17], v[28:31], v[126:129], v[2:17]
	ds_read_b128 v[28:31], v168 offset:4096
	s_waitcnt lgkmcnt(0)
	v_mfma_f32_32x32x16_bf16 v[66:81], v[28:31], v[126:129], v[66:81]
	s_cbranch_scc1 .LBB0_841
	s_setprio 1
; #define LAS __attribute__((address_space(3)))
; __device__ __forceinline__ int v_rd_base(int lane) { return ((lane & 3) << 3) | (((lane >> 2) & 3) << 6) | (((lane >> 4) & 1) << 5) | (((lane >> 5) & 1) << 8); }
; #define DMA_WAIT(last) do { if (last) asm volatile("s_waitcnt vmcnt(0)" ::: "memory"); else asm volatile("s_waitcnt vmcnt(%0)" :: "n"(NPW) : "memory"); } while (0)
; template <int DK, int DV, bool OFF, class QLoader> ...
;     ...
;   float l_reg = 0; f32x16 o[ND];
; #pragma unroll
;   for (int d = 0; d < ND; ++d) o[d] = f32x16{};
;   bf16x8 qr[DK / 16];
;   QL.load(qr, wid * QBLK + r32, hi);
;   asm volatile("s_waitcnt vmcnt(0)" ::: "memory");
;   unsigned koff[KPW], voff[VPW];
; #pragma unroll
;   for (int i = 0; i < (DK == 64 ? 1 : KPW); ++i) { const int row = (wid * KPW + i) * 4 + (lane >> 4); int c = (lane & 15) ^ (row & 7); c = (c < DK / 8) ? c : (c & 7); koff[i] = (unsigned)((row * ldk) * 2 + c * 16); }
; #pragma unroll
;   for (int i = 0; i < 1; ++i) { const int sidx = (wid * VPW + i) * 2 + (lane >> 5), kg = sidx / ND, st = sidx % ND, kk = kg * 8 + ((lane & 31) >> 2);
;     const int k = (kk & ~0xC) | ((kk & 4) << 1) | ((kk & 8) >> 1), c = st * 32 + (lane & 3) * 8; voff[i] = (unsigned)((k * ldv + c) * 2); }
;   const int vb0 = (int)(uintptr_t)V_lds + v_rd_base(lane);
;   LAS unsigned* const ldsK = (LAS unsigned*)(LAS char*)K_lds + (wid * KPW) * 256; LAS unsigned* const ldsV = (LAS unsigned*)(LAS char*)V_lds + (wid * VPW) * 256;
;     ...
;   f32x16 pA0, pA1, pB0, pB1; bf16x8 pa0, pa1, pa2, pa3; const int NT = nkeys / KVBLK;
;   DMA_TILE(0, 0); DMA_TILE(1, 1); DMA_WAIT(false); __syncthreads(); if (2 < NT) DMA_TILE(2, 2);
;   qkt<DK>(pA0, pA1, K_lds, qr, r32, hi); partialSM<DK, OFF>(pA0, pA1, negMC);
;     ...
;   if (wid >= 4) __builtin_amdgcn_s_setprio(1);
;   for (int j = 1; j < NT; j += 4) {
.LBB0_841:
	s_add_u32 s93, s16, 0x8000
	v_and_b32_e32 v25, 63, v25
	s_addc_u32 s94, s17, 0
	s_nop 4
	v_exp_f32_e32 v174, v3
	s_and_b64 s[24:25], s[14:15], exec
	v_lshlrev_b32_e32 v3, 4, v25
	v_exp_f32_e32 v173, v2
	v_exp_f32_e32 v175, v4
	s_cselect_b32 s95, 0x44, 4
	v_lshlrev_b32_e32 v2, 3, v25
	v_and_b32_e32 v3, 0xc0, v3
	v_lshlrev_b32_e32 v4, 1, v25
	s_cmp_lg_u32 0, -1
	v_and_or_b32 v3, v2, 24, v3
	v_and_b32_e32 v4, 32, v4
	v_and_b32_e32 v2, 0x100, v2
	s_cselect_b32 s24, 0, 0
	v_or3_b32 v2, v3, v4, v2
	s_add_i32 s25, s24, 0x4000
	v_add_u32_e32 v169, s24, v2
	v_add_u32_e32 v170, s25, v2
	s_add_i32 s25, s24, 0x8000
	s_add_i32 s24, s24, 0xc000
	v_add_u32_e32 v160, s24, v2
	s_and_b32 s24, s76, 14
	v_add_u32_e32 v171, s25, v2
	s_lshl_b32 s26, s24, 7
	v_add3_u32 v2, v22, v23, v26
	s_movk_i32 s24, 0xc00
	s_add_i32 s96, s95, -1
	s_add_i32 s97, s95, -3
	s_add_i32 s59, s95, -4
	v_mul_lo_u32 v2, v2, s24
	s_add_u32 s2, s2, s26
	v_lshl_add_u32 v2, v20, 5, v2
	v_readlane_b32 s28, v251, 4
	s_addc_u32 s4, s4, 0
	v_or_b32_e32 v2, v2, v24
	v_lshlrev_b32_e32 v3, 7, v21
	v_readlane_b32 s30, v251, 6
	v_sub_u32_e32 v2, v2, v3
	v_readlane_b32 s31, v251, 7
	s_add_u32 s24, s30, s2
	v_lshlrev_b32_e32 v2, 1, v2
	v_mov_b32_e32 v3, v1
	s_addc_u32 s25, s31, s4
	v_lshl_add_u64 v[152:153], s[24:25], 0, v[2:3]
	s_add_u32 s24, s30, s78
	s_addc_u32 s25, s31, s77
	v_readlane_b32 s2, v253, 21
	s_add_u32 s60, s2, s78
	v_readlane_b32 s2, v253, 22
	s_addc_u32 s45, s2, s77
	v_exp_f32_e32 v184, v5
	v_exp_f32_e32 v185, v6
	v_exp_f32_e32 v186, v7
	v_exp_f32_e32 v187, v8
	v_exp_f32_e32 v188, v9
	v_exp_f32_e32 v189, v10
	v_exp_f32_e32 v190, v11
	v_exp_f32_e32 v191, v12
	v_exp_f32_e32 v192, v13
	v_exp_f32_e32 v193, v14
	v_exp_f32_e32 v194, v15
	v_exp_f32_e32 v195, v16
	v_exp_f32_e32 v196, v17
	s_add_u32 s2, s80, s26
	v_mov_b32_e32 v2, v0
	s_addc_u32 s5, s79, 0
	v_readlane_b32 s4, v253, 23
	v_mov_b32_e32 v16, v1
	v_mov_b32_e32 v17, v1
	v_lshl_add_u64 v[156:157], s[24:25], 0, v[2:3]
	s_add_u32 s4, s4, s2
	v_readlane_b32 s2, v253, 24
	v_mov_b32_e32 v2, v1
	v_mov_b32_e32 v4, v1
	v_mov_b32_e32 v5, v1
	v_mov_b32_e32 v6, v1
	v_mov_b32_e32 v7, v1
	v_mov_b32_e32 v8, v1
	v_mov_b32_e32 v9, v1
	v_mov_b32_e32 v10, v1
	v_mov_b32_e32 v11, v1
	v_mov_b32_e32 v12, v1
	v_mov_b32_e32 v13, v1
	v_mov_b32_e32 v14, v1
	v_mov_b32_e32 v15, v1
	v_mov_b64_e32 v[64:65], v[16:17]
	v_mov_b64_e32 v[48:49], v[16:17]
	v_mov_b64_e32 v[32:33], v[16:17]
	v_lshl_add_u64 v[154:155], s[24:25], 0, v[150:151]
	s_addc_u32 s5, s2, s5
	v_mov_b32_e32 v172, 0
	s_mov_b32 s55, 6
	s_movk_i32 s2, 0xffc0
	v_mov_b64_e32 v[62:63], v[14:15]
	v_mov_b64_e32 v[60:61], v[12:13]
	v_mov_b64_e32 v[58:59], v[10:11]
	v_mov_b64_e32 v[56:57], v[8:9]
	v_mov_b64_e32 v[54:55], v[6:7]
	v_mov_b64_e32 v[52:53], v[4:5]
	v_mov_b64_e32 v[50:51], v[2:3]
	v_mov_b64_e32 v[46:47], v[14:15]
	v_mov_b64_e32 v[44:45], v[12:13]
	v_mov_b64_e32 v[42:43], v[10:11]
	v_mov_b64_e32 v[40:41], v[8:9]
	v_mov_b64_e32 v[38:39], v[6:7]
	v_mov_b64_e32 v[36:37], v[4:5]
	v_mov_b64_e32 v[34:35], v[2:3]
	v_mov_b64_e32 v[30:31], v[14:15]
	v_mov_b64_e32 v[28:29], v[12:13]
	v_mov_b64_e32 v[26:27], v[10:11]
	v_mov_b64_e32 v[24:25], v[8:9]
	v_mov_b64_e32 v[22:23], v[6:7]
	v_mov_b64_e32 v[20:21], v[4:5]
	v_mov_b64_e32 v[18:19], v[2:3]
	v_readlane_b32 s29, v251, 5

; #define DMA_WAIT(last) do { if (last) asm volatile("s_waitcnt vmcnt(0)" ::: "memory"); else asm volatile("s_waitcnt vmcnt(%0)" :: "n"(NPW) : "memory"); } while (0)
; template <int DK>
; __device__ __forceinline__ void qkt(f32x16& p0, f32x16& p1, const char* Ks, const bf16x8* qr, int r32, int hi) {
;   p0 = f32x16{}; p1 = f32x16{};
; #pragma unroll
;   for (int d0 = 0; d0 < DK / 16; ++d0) { const int cb = (d0 * 16 + hi * 8) * 2;
;     const bf16x8 b0 = *reinterpret_cast<const bf16x8*>(Ks + ATT_KSWZ(r32, cb));
;     const bf16x8 b1 = *reinterpret_cast<const bf16x8*>(Ks + ATT_KSWZ(32 + r32, cb));
;     p0 = __builtin_amdgcn_mfma_f32_32x32x16_bf16(b0, qr[d0], p0, 0, 0, 0);
;     p1 = __builtin_amdgcn_mfma_f32_32x32x16_bf16(b1, qr[d0], p1, 0, 0, 0);
;   }
; }
; template <int DK, int DV, bool OFF, class QLoader> ...
;     ...
;   f32x16 pA0, pA1, pB0, pB1; bf16x8 pa0, pa1, pa2, pa3; const int NT = nkeys / KVBLK;
;   DMA_TILE(0, 0); DMA_TILE(1, 1); DMA_WAIT(false); __syncthreads(); if (2 < NT) DMA_TILE(2, 2);
;   qkt<DK>(pA0, pA1, K_lds, qr, r32, hi); partialSM<DK, OFF>(pA0, pA1, negMC);
.LBB0_855:
	v_lshl_add_u64 v[82:83], s[30:31], 0, v[0:1]
	s_add_i32 m0, s81, 0xc000
	s_nop 0
	global_load_lds_dwordx4 v[82:83], off
	v_lshl_add_u64 v[82:83], s[36:37], 0, v[148:149]
	s_add_i32 m0, s82, 0xc000
	s_nop 0
	global_load_lds_dwordx4 v[82:83], off
	v_lshl_add_u64 v[82:83], v[82:83], 0, s[10:11]
	s_add_i32 m0, s82, 0xc400
	s_nop 0
	global_load_lds_dwordx4 v[82:83], off
.LBB0_856:
	ds_read_b128 v[82:85], v162 offset:16384
	ds_read_b128 v[86:89], v162 offset:20480
	ds_read_b128 v[130:133], v164 offset:16384
	ds_read_b128 v[134:137], v164 offset:20480
	v_exp_f32_e32 v66, v66
	v_add_f32_e32 v180, 0, v173
	v_add_f32_e32 v180, v174, v180
	v_add_f32_e32 v180, v175, v180
	v_add_f32_e32 v180, v184, v180
	v_add_f32_e32 v180, v185, v180
	v_add_f32_e32 v180, v186, v180
	v_add_f32_e32 v180, v187, v180
	v_add_f32_e32 v180, v188, v180
	v_add_f32_e32 v180, v189, v180
	v_add_f32_e32 v180, v190, v180
	v_add_f32_e32 v180, v191, v180
	v_add_f32_e32 v180, v192, v180
	v_add_f32_e32 v180, v193, v180
	v_add_f32_e32 v180, v194, v180
	v_add_f32_e32 v180, v195, v180
	v_add_f32_e32 v180, v196, v180
	s_waitcnt lgkmcnt(0)
	v_mfma_f32_32x32x16_bf16 v[98:113], v[82:85], v[114:117], 0
	v_exp_f32_e32 v67, v67
	v_exp_f32_e32 v68, v68
	v_exp_f32_e32 v69, v69
	v_exp_f32_e32 v70, v70
	v_exp_f32_e32 v71, v71
	v_exp_f32_e32 v72, v72
	v_exp_f32_e32 v73, v73
	v_mfma_f32_32x32x16_bf16 v[82:97], v[86:89], v[114:117], 0
	v_exp_f32_e32 v74, v74
	v_exp_f32_e32 v75, v75
	v_exp_f32_e32 v76, v76
	v_exp_f32_e32 v77, v77
	v_exp_f32_e32 v78, v78
	v_exp_f32_e32 v79, v79
	v_exp_f32_e32 v80, v80
	v_mfma_f32_32x32x16_bf16 v[98:113], v[130:133], v[118:121], v[98:113]
	v_exp_f32_e32 v81, v81
	s_andn2_b64 vcc, exec, s[26:27]
	v_mfma_f32_32x32x16_bf16 v[82:97], v[134:137], v[118:121], v[82:97]
	ds_read_b128 v[130:133], v166 offset:16384
	ds_read_b128 v[134:137], v166 offset:20480
	v_add_f32_e32 v180, v66, v180
	v_add_f32_e32 v180, v67, v180
	v_add_f32_e32 v180, v68, v180
	v_add_f32_e32 v180, v69, v180
	v_add_f32_e32 v180, v70, v180
	v_add_f32_e32 v180, v71, v180
	v_add_f32_e32 v180, v72, v180
	v_add_f32_e32 v180, v73, v180
	s_waitcnt lgkmcnt(0)
	v_mfma_f32_32x32x16_bf16 v[98:113], v[130:133], v[122:125], v[98:113]
	v_mfma_f32_32x32x16_bf16 v[82:97], v[134:137], v[122:125], v[82:97]
	ds_read_b128 v[130:133], v168 offset:16384
	ds_read_b128 v[134:137], v168 offset:20480
	v_add_f32_e32 v180, v74, v180
	v_add_f32_e32 v180, v75, v180
	v_add_f32_e32 v180, v76, v180
	v_add_f32_e32 v180, v77, v180
	v_add_f32_e32 v180, v78, v180
	v_add_f32_e32 v180, v79, v180
	v_add_f32_e32 v180, v80, v180
	v_add_f32_e32 v180, v81, v180
	s_waitcnt lgkmcnt(0)
	v_mfma_f32_32x32x16_bf16 v[98:113], v[130:133], v[126:129], v[98:113]
	v_mfma_f32_32x32x16_bf16 v[82:97], v[134:137], v[126:129], v[82:97]
	v_add_f32_e32 v172, v172, v180
	v_cvt_pk_bf16_f32 v130, v173, v174
	v_cvt_pk_bf16_f32 v131, v175, v184
	v_cvt_pk_bf16_f32 v132, v185, v186
	v_cvt_pk_bf16_f32 v133, v187, v188
	v_cvt_pk_bf16_f32 v134, v189, v190
	v_cvt_pk_bf16_f32 v135, v191, v192
	v_cvt_pk_bf16_f32 v136, v193, v194
	v_cvt_pk_bf16_f32 v137, v195, v196
	v_cvt_pk_bf16_f32 v138, v66, v67
	v_cvt_pk_bf16_f32 v139, v68, v69
	v_cvt_pk_bf16_f32 v140, v70, v71
	v_cvt_pk_bf16_f32 v141, v72, v73
	v_cvt_pk_bf16_f32 v142, v74, v75
	v_cvt_pk_bf16_f32 v143, v76, v77
	v_cvt_pk_bf16_f32 v144, v78, v79
	v_cvt_pk_bf16_f32 v145, v80, v81
	ds_read_b64_tr_b16 v[176:177], v169 offset:0
	ds_read_b64_tr_b16 v[178:179], v169 offset:0x800
	ds_read_b64_tr_b16 v[198:199], v169 offset:0x1000
	ds_read_b64_tr_b16 v[200:201], v169 offset:0x1800
	ds_read_b64_tr_b16 v[202:203], v169 offset:0x2000
	ds_read_b64_tr_b16 v[204:205], v169 offset:0x2800
	ds_read_b64_tr_b16 v[206:207], v169 offset:0x3000
	ds_read_b64_tr_b16 v[208:209], v169 offset:0x3800
	ds_read_b64_tr_b16 v[210:211], v169 offset:0x200
	ds_read_b64_tr_b16 v[212:213], v169 offset:0xa00
	ds_read_b64_tr_b16 v[214:215], v169 offset:0x1200
	s_nop 0
	v_permlane32_swap_b32_e32 v130, v132
	v_permlane32_swap_b32_e32 v131, v133
	ds_read_b64_tr_b16 v[216:217], v169 offset:0x1a00
	ds_read_b64_tr_b16 v[218:219], v169 offset:0x2200
	ds_read_b64_tr_b16 v[220:221], v169 offset:0x2a00
	ds_read_b64_tr_b16 v[222:223], v169 offset:0x3200
	ds_read_b64_tr_b16 v[224:225], v169 offset:0x3a00
	s_waitcnt lgkmcnt(8)
	v_permlane32_swap_b32_e32 v134, v136
	s_nop 0
	v_mfma_f32_32x32x16_bf16 v[2:17], v[130:133], v[176:179], v[2:17]
	v_permlane32_swap_b32_e32 v135, v137
	v_permlane32_swap_b32_e32 v138, v140
	v_permlane32_swap_b32_e32 v139, v141
	ds_read_b64_tr_b16 v[176:177], v169 offset:0x400
	v_mfma_f32_32x32x16_bf16 v[2:17], v[134:137], v[198:201], v[2:17]
	v_permlane32_swap_b32_e32 v142, v144
	v_permlane32_swap_b32_e32 v143, v145
	ds_read_b64_tr_b16 v[178:179], v169 offset:0xc00
	ds_read_b64_tr_b16 v[198:199], v169 offset:0x1400
	ds_read_b64_tr_b16 v[200:201], v169 offset:0x1c00
	v_mfma_f32_32x32x16_bf16 v[2:17], v[138:141], v[202:205], v[2:17]
	ds_read_b64_tr_b16 v[202:203], v169 offset:0x2400
	ds_read_b64_tr_b16 v[204:205], v169 offset:0x2c00
	v_exp_f32_e32 v197, v98
	v_mfma_f32_32x32x16_bf16 v[2:17], v[142:145], v[206:209], v[2:17]
	ds_read_b64_tr_b16 v[206:207], v169 offset:0x3400
	ds_read_b64_tr_b16 v[208:209], v169 offset:0x3c00
	s_waitcnt lgkmcnt(8)
	s_nop 0
	v_mfma_f32_32x32x16_bf16 v[50:65], v[130:133], v[210:213], v[50:65]
	ds_read_b64_tr_b16 v[210:211], v169 offset:0x600
	ds_read_b64_tr_b16 v[212:213], v169 offset:0xe00
	v_mfma_f32_32x32x16_bf16 v[50:65], v[134:137], v[214:217], v[50:65]
	ds_read_b64_tr_b16 v[214:215], v169 offset:0x1600
	ds_read_b64_tr_b16 v[216:217], v169 offset:0x1e00
	v_mfma_f32_32x32x16_bf16 v[50:65], v[138:141], v[218:221], v[50:65]
	ds_read_b64_tr_b16 v[218:219], v169 offset:0x2600
	ds_read_b64_tr_b16 v[220:221], v169 offset:0x2e00
	v_mfma_f32_32x32x16_bf16 v[50:65], v[142:145], v[222:225], v[50:65]
	ds_read_b64_tr_b16 v[222:223], v169 offset:0x3600
	ds_read_b64_tr_b16 v[224:225], v169 offset:0x3e00
	s_waitcnt lgkmcnt(8)
	s_nop 0
	s_waitcnt lgkmcnt(0)
	v_mfma_f32_32x32x16_bf16 v[34:49], v[130:133], v[176:179], v[34:49]
	v_mfma_f32_32x32x16_bf16 v[18:33], v[130:133], v[210:213], v[18:33]
	v_exp_f32_e32 v210, v105
	v_exp_f32_e32 v211, v111
	v_exp_f32_e32 v212, v113
	v_mfma_f32_32x32x16_bf16 v[34:49], v[134:137], v[198:201], v[34:49]
	v_exp_f32_e32 v200, v99
	v_exp_f32_e32 v198, v100
	v_exp_f32_e32 v199, v106
	v_exp_f32_e32 v201, v108
	v_mfma_f32_32x32x16_bf16 v[18:33], v[134:137], v[214:217], v[18:33]
	v_mfma_f32_32x32x16_bf16 v[34:49], v[138:141], v[202:205], v[34:49]
	v_exp_f32_e32 v202, v101
	v_exp_f32_e32 v204, v102
	v_exp_f32_e32 v205, v104
	v_exp_f32_e32 v203, v107
	v_mfma_f32_32x32x16_bf16 v[18:33], v[138:141], v[218:221], v[18:33]
	v_mfma_f32_32x32x16_bf16 v[34:49], v[142:145], v[206:209], v[34:49]
	v_exp_f32_e32 v207, v103
	v_exp_f32_e32 v209, v109
	v_exp_f32_e32 v206, v110
	v_exp_f32_e32 v208, v112
	v_mfma_f32_32x32x16_bf16 v[18:33], v[142:145], v[222:225], v[18:33]
	s_cbranch_vccnz .LBB0_865
; #define DMA_WAIT(last) do { if (last) asm volatile("s_waitcnt vmcnt(0)" ::: "memory"); else asm volatile("s_waitcnt vmcnt(%0)" :: "n"(NPW) : "memory"); } while (0)
; template <int DK, int DV, bool OFF, class QLoader> ...
;     ...
;   f32x16 pA0, pA1, pB0, pB1; bf16x8 pa0, pa1, pa2, pa3; const int NT = nkeys / KVBLK;
;   DMA_TILE(0, 0); DMA_TILE(1, 1); DMA_WAIT(false); __syncthreads(); if (2 < NT) DMA_TILE(2, 2);
;   qkt<DK>(pA0, pA1, K_lds, qr, r32, hi); partialSM<DK, OFF>(pA0, pA1, negMC);
.LBB0_859:
.LBB0_861:
	s_add_i32 s26, s55, -2
	s_cmp_ge_u32 s26, s95
	s_waitcnt vmcnt(0)
	s_barrier
	s_cbranch_scc1 .LBB0_863
	v_lshl_add_u64 v[66:67], v[156:157], 0, s[8:9]
	s_mov_b64 s[26:27], 0x1ec08000
	s_mov_b32 m0, s81
	v_lshl_add_u64 v[66:67], v[66:67], 0, s[26:27]
	global_load_lds_dwordx4 v[66:67], off
	s_mov_b64 s[26:27], 0xdc01000
	v_lshl_add_u64 v[66:67], v[152:153], 0, s[8:9]
	v_lshl_add_u64 v[68:69], v[66:67], 0, s[26:27]
	s_mov_b32 m0, s82
	s_mov_b64 s[26:27], 0xdc01080
	global_load_lds_dwordx4 v[68:69], off
	v_lshl_add_u64 v[66:67], v[66:67], 0, s[26:27]
	s_mov_b32 m0, s84
	s_nop 0
	global_load_lds_dwordx4 v[66:67], off
; template <int DK>
; __device__ __forceinline__ void qkt(f32x16& p0, f32x16& p1, const char* Ks, const bf16x8* qr, int r32, int hi) {
;   p0 = f32x16{}; p1 = f32x16{};
; #pragma unroll
;   for (int d0 = 0; d0 < DK / 16; ++d0) { const int cb = (d0 * 16 + hi * 8) * 2;
;     const bf16x8 b0 = *reinterpret_cast<const bf16x8*>(Ks + ATT_KSWZ(r32, cb));
;     const bf16x8 b1 = *reinterpret_cast<const bf16x8*>(Ks + ATT_KSWZ(32 + r32, cb));
;     p0 = __builtin_amdgcn_mfma_f32_32x32x16_bf16(b0, qr[d0], p0, 0, 0, 0);
;     p1 = __builtin_amdgcn_mfma_f32_32x32x16_bf16(b1, qr[d0], p1, 0, 0, 0);
;   }
; }
.LBB0_863:
	ds_read_b128 v[66:69], v162 offset:32768
	ds_read_b128 v[70:73], v162 offset:36864
	ds_read_b128 v[130:133], v164 offset:32768
	ds_read_b128 v[134:137], v164 offset:36864
	v_exp_f32_e32 v82, v82
	v_add_f32_e32 v180, 0, v197
	v_add_f32_e32 v180, v200, v180
	v_add_f32_e32 v180, v198, v180
	v_add_f32_e32 v180, v202, v180
	v_add_f32_e32 v180, v204, v180
	v_add_f32_e32 v180, v207, v180
	v_add_f32_e32 v180, v205, v180
	v_add_f32_e32 v180, v210, v180
	v_add_f32_e32 v180, v199, v180
	v_add_f32_e32 v180, v203, v180
	v_add_f32_e32 v180, v201, v180
	v_add_f32_e32 v180, v209, v180
	v_add_f32_e32 v180, v206, v180
	v_add_f32_e32 v180, v211, v180
	v_add_f32_e32 v180, v208, v180
	v_add_f32_e32 v180, v212, v180
	s_waitcnt lgkmcnt(0)
	v_mfma_f32_32x32x16_bf16 v[98:113], v[66:69], v[114:117], 0
	v_exp_f32_e32 v83, v83
	v_exp_f32_e32 v84, v84
	v_exp_f32_e32 v85, v85
	v_exp_f32_e32 v86, v86
	v_exp_f32_e32 v87, v87
	v_exp_f32_e32 v88, v88
	v_exp_f32_e32 v89, v89
	v_mfma_f32_32x32x16_bf16 v[66:81], v[70:73], v[114:117], 0
	v_exp_f32_e32 v90, v90
	v_exp_f32_e32 v91, v91
	v_exp_f32_e32 v92, v92
	v_exp_f32_e32 v93, v93
	v_exp_f32_e32 v94, v94
	v_exp_f32_e32 v95, v95
	v_exp_f32_e32 v96, v96
	v_mfma_f32_32x32x16_bf16 v[98:113], v[130:133], v[118:121], v[98:113]
	v_exp_f32_e32 v97, v97
	v_mfma_f32_32x32x16_bf16 v[66:81], v[134:137], v[118:121], v[66:81]
	ds_read_b128 v[130:133], v166 offset:32768
	ds_read_b128 v[134:137], v166 offset:36864
	v_add_f32_e32 v180, v82, v180
	v_add_f32_e32 v180, v83, v180
	v_add_f32_e32 v180, v84, v180
	v_add_f32_e32 v180, v85, v180
	v_add_f32_e32 v180, v86, v180
	v_add_f32_e32 v180, v87, v180
	v_add_f32_e32 v180, v88, v180
	v_add_f32_e32 v180, v89, v180
	s_waitcnt lgkmcnt(0)
	v_mfma_f32_32x32x16_bf16 v[98:113], v[130:133], v[122:125], v[98:113]
	v_mfma_f32_32x32x16_bf16 v[66:81], v[134:137], v[122:125], v[66:81]
	ds_read_b128 v[130:133], v168 offset:32768
	ds_read_b128 v[134:137], v168 offset:36864
	v_add_f32_e32 v180, v90, v180
	v_add_f32_e32 v180, v91, v180
	v_add_f32_e32 v180, v92, v180
	v_add_f32_e32 v180, v93, v180
	v_add_f32_e32 v180, v94, v180
	v_add_f32_e32 v180, v95, v180
	v_add_f32_e32 v180, v96, v180
	v_add_f32_e32 v180, v97, v180
	s_waitcnt lgkmcnt(0)
	v_mfma_f32_32x32x16_bf16 v[98:113], v[130:133], v[126:129], v[98:113]
	v_mfma_f32_32x32x16_bf16 v[66:81], v[134:137], v[126:129], v[66:81]
	v_add_f32_e32 v172, v172, v180
	v_cvt_pk_bf16_f32 v130, v197, v200
	v_cvt_pk_bf16_f32 v131, v198, v202
	v_cvt_pk_bf16_f32 v132, v204, v207
	v_cvt_pk_bf16_f32 v133, v205, v210
	v_cvt_pk_bf16_f32 v134, v199, v203
	v_cvt_pk_bf16_f32 v135, v201, v209
	v_cvt_pk_bf16_f32 v136, v206, v211
	v_cvt_pk_bf16_f32 v137, v208, v212
	v_cvt_pk_bf16_f32 v138, v82, v83
	v_cvt_pk_bf16_f32 v139, v84, v85
	v_cvt_pk_bf16_f32 v140, v86, v87
	v_cvt_pk_bf16_f32 v141, v88, v89
	v_cvt_pk_bf16_f32 v142, v90, v91
	v_cvt_pk_bf16_f32 v143, v92, v93
	v_cvt_pk_bf16_f32 v144, v94, v95
	v_cvt_pk_bf16_f32 v145, v96, v97
	ds_read_b64_tr_b16 v[174:175], v170 offset:0
	ds_read_b64_tr_b16 v[176:177], v170 offset:0x800
	ds_read_b64_tr_b16 v[184:185], v170 offset:0x1000
	ds_read_b64_tr_b16 v[186:187], v170 offset:0x1800
	ds_read_b64_tr_b16 v[188:189], v170 offset:0x2000
	ds_read_b64_tr_b16 v[190:191], v170 offset:0x2800
	ds_read_b64_tr_b16 v[192:193], v170 offset:0x3000
	ds_read_b64_tr_b16 v[194:195], v170 offset:0x3800
	ds_read_b64_tr_b16 v[214:215], v170 offset:0x200
	ds_read_b64_tr_b16 v[216:217], v170 offset:0xa00
	ds_read_b64_tr_b16 v[218:219], v170 offset:0x1200
	s_nop 0
	v_permlane32_swap_b32_e32 v130, v132
	v_permlane32_swap_b32_e32 v131, v133
	ds_read_b64_tr_b16 v[220:221], v170 offset:0x1a00
	ds_read_b64_tr_b16 v[222:223], v170 offset:0x2200
	ds_read_b64_tr_b16 v[224:225], v170 offset:0x2a00
	ds_read_b64_tr_b16 v[226:227], v170 offset:0x3200
	ds_read_b64_tr_b16 v[228:229], v170 offset:0x3a00
	s_waitcnt lgkmcnt(8)
	v_permlane32_swap_b32_e32 v134, v136
	s_nop 0
	v_mfma_f32_32x32x16_bf16 v[2:17], v[130:133], v[174:177], v[2:17]
	v_permlane32_swap_b32_e32 v135, v137
	v_permlane32_swap_b32_e32 v138, v140
	v_permlane32_swap_b32_e32 v139, v141
	ds_read_b64_tr_b16 v[174:175], v170 offset:0x400
	v_mfma_f32_32x32x16_bf16 v[2:17], v[134:137], v[184:187], v[2:17]
	v_permlane32_swap_b32_e32 v142, v144
	v_permlane32_swap_b32_e32 v143, v145
	ds_read_b64_tr_b16 v[176:177], v170 offset:0xc00
	ds_read_b64_tr_b16 v[184:185], v170 offset:0x1400
	ds_read_b64_tr_b16 v[186:187], v170 offset:0x1c00
	v_mfma_f32_32x32x16_bf16 v[2:17], v[138:141], v[188:191], v[2:17]
	ds_read_b64_tr_b16 v[188:189], v170 offset:0x2400
	ds_read_b64_tr_b16 v[190:191], v170 offset:0x2c00
	v_exp_f32_e32 v173, v98
	v_exp_f32_e32 v196, v113
	v_mfma_f32_32x32x16_bf16 v[2:17], v[142:145], v[192:195], v[2:17]
	ds_read_b64_tr_b16 v[192:193], v170 offset:0x3400
	ds_read_b64_tr_b16 v[194:195], v170 offset:0x3c00
	s_waitcnt lgkmcnt(8)
	s_nop 0
	v_mfma_f32_32x32x16_bf16 v[50:65], v[130:133], v[214:217], v[50:65]
	ds_read_b64_tr_b16 v[214:215], v170 offset:0x600
	ds_read_b64_tr_b16 v[216:217], v170 offset:0xe00
	v_mfma_f32_32x32x16_bf16 v[50:65], v[134:137], v[218:221], v[50:65]
	ds_read_b64_tr_b16 v[218:219], v170 offset:0x1600
	ds_read_b64_tr_b16 v[220:221], v170 offset:0x1e00
	v_mfma_f32_32x32x16_bf16 v[50:65], v[138:141], v[222:225], v[50:65]
	ds_read_b64_tr_b16 v[222:223], v170 offset:0x2600
	ds_read_b64_tr_b16 v[224:225], v170 offset:0x2e00
	v_mfma_f32_32x32x16_bf16 v[50:65], v[142:145], v[226:229], v[50:65]
	ds_read_b64_tr_b16 v[226:227], v170 offset:0x3600
	ds_read_b64_tr_b16 v[228:229], v170 offset:0x3e00
	s_waitcnt lgkmcnt(8)
	s_nop 0
	s_waitcnt lgkmcnt(0)
	v_mfma_f32_32x32x16_bf16 v[34:49], v[130:133], v[174:177], v[34:49]
	v_exp_f32_e32 v174, v99
	v_exp_f32_e32 v175, v100
	v_mfma_f32_32x32x16_bf16 v[18:33], v[130:133], v[214:217], v[18:33]
	v_mfma_f32_32x32x16_bf16 v[34:49], v[134:137], v[184:187], v[34:49]
	v_exp_f32_e32 v184, v101
	v_exp_f32_e32 v185, v102
	v_exp_f32_e32 v186, v103
	v_exp_f32_e32 v187, v104
	v_mfma_f32_32x32x16_bf16 v[18:33], v[134:137], v[218:221], v[18:33]
	v_mfma_f32_32x32x16_bf16 v[34:49], v[138:141], v[188:191], v[34:49]
	v_exp_f32_e32 v188, v105
	v_exp_f32_e32 v189, v106
	v_exp_f32_e32 v190, v107
	v_exp_f32_e32 v191, v108
	v_mfma_f32_32x32x16_bf16 v[18:33], v[138:141], v[222:225], v[18:33]
	v_mfma_f32_32x32x16_bf16 v[34:49], v[142:145], v[192:195], v[34:49]
	v_exp_f32_e32 v192, v109
	v_exp_f32_e32 v193, v110
	v_exp_f32_e32 v194, v111
	v_exp_f32_e32 v195, v112
	v_mfma_f32_32x32x16_bf16 v[18:33], v[142:145], v[226:229], v[18:33]
	s_andn2_b64 vcc, exec, s[24:25]
	s_cbranch_vccz .LBB0_866

; #define DMA_WAIT(last) do { if (last) asm volatile("s_waitcnt vmcnt(0)" ::: "memory"); else asm volatile("s_waitcnt vmcnt(%0)" :: "n"(NPW) : "memory"); } while (0)
; template <int DK, int DV, bool OFF, class QLoader> ...
;     ...
;   f32x16 pA0, pA1, pB0, pB1; bf16x8 pa0, pa1, pa2, pa3; const int NT = nkeys / KVBLK;
;   DMA_TILE(0, 0); DMA_TILE(1, 1); DMA_WAIT(false); __syncthreads(); if (2 < NT) DMA_TILE(2, 2);
;   qkt<DK>(pA0, pA1, K_lds, qr, r32, hi); partialSM<DK, OFF>(pA0, pA1, negMC);
.LBB0_868:
.LBB0_870:
	s_add_i32 s24, s55, -1
	s_cmp_ge_u32 s24, s95
	s_waitcnt vmcnt(0)
	s_barrier
	s_cbranch_scc1 .LBB0_872
	v_lshl_add_u64 v[82:83], v[156:157], 0, s[8:9]
	s_mov_b64 s[24:25], 0x1ec0a000
	s_mov_b32 m0, s85
	v_lshl_add_u64 v[82:83], v[82:83], 0, s[24:25]
	global_load_lds_dwordx4 v[82:83], off
	s_mov_b64 s[24:25], 0xdc61000
	v_lshl_add_u64 v[82:83], v[152:153], 0, s[8:9]
	v_lshl_add_u64 v[84:85], v[82:83], 0, s[24:25]
	s_mov_b32 m0, s87
	s_mov_b64 s[24:25], 0xdc61080
	global_load_lds_dwordx4 v[84:85], off
	v_lshl_add_u64 v[82:83], v[82:83], 0, s[24:25]
	s_mov_b32 m0, s88
	s_nop 0
	global_load_lds_dwordx4 v[82:83], off
; __device__ __forceinline__ void finishSM(f32x16& p0, f32x16& p1, float& l_reg, bf16x8& pa0, bf16x8& pa1, bf16x8& pa2, bf16x8& pa3) {
; #pragma unroll
;   for (int r = 0; r < 16; ++r) p1[r] = __builtin_amdgcn_exp2f(p1[r]);
;   float ps = 0;
; #pragma unroll
;   for (int r = 0; r < 16; ++r) ps += p0[r];
; #pragma unroll
;   for (int r = 0; r < 16; ++r) ps += p1[r];
;   l_reg += ps;
;     ...
;   ATT_PK4(p0, 0, pa0); ATT_PK4(p0, 8, pa1); ATT_PK4(p1, 0, pa2); ATT_PK4(p1, 8, pa3);
;     ...
; }
; template <int DK>
; __device__ __forceinline__ void qkt(f32x16& p0, f32x16& p1, const char* Ks, const bf16x8* qr, int r32, int hi) {
;   p0 = f32x16{}; p1 = f32x16{};
; #pragma unroll
;   for (int d0 = 0; d0 < DK / 16; ++d0) { const int cb = (d0 * 16 + hi * 8) * 2;
;     const bf16x8 b0 = *reinterpret_cast<const bf16x8*>(Ks + ATT_KSWZ(r32, cb));
;     const bf16x8 b1 = *reinterpret_cast<const bf16x8*>(Ks + ATT_KSWZ(32 + r32, cb));
;     p0 = __builtin_amdgcn_mfma_f32_32x32x16_bf16(b0, qr[d0], p0, 0, 0, 0);
;     p1 = __builtin_amdgcn_mfma_f32_32x32x16_bf16(b1, qr[d0], p1, 0, 0, 0);
;   }
; }
; template <int DV, int GRP> __device__ __forceinline__ void v_group_read(s16x4* vf, int vb) {
;   sfor<0, 8>([&](auto ic) { constexpr int j = decltype(ic)::value; vf[j] = tr_read<v_rd_off<DV>(GRP, j / 2, j % 2)>(vb); });
; }
; __device__ __forceinline__ void pv_group(f32x16& od, const s16x4* vf, bf16x8 pa0, bf16x8 pa1, bf16x8 pa2, bf16x8 pa3) {
;     ...
;   od = __builtin_amdgcn_mfma_f32_32x32x16_bf16(pa0, ATT_PK(vf[0], vf[1]), od, 0, 0, 0);
;   od = __builtin_amdgcn_mfma_f32_32x32x16_bf16(pa1, ATT_PK(vf[2], vf[3]), od, 0, 0, 0);
;   od = __builtin_amdgcn_mfma_f32_32x32x16_bf16(pa2, ATT_PK(vf[4], vf[5]), od, 0, 0, 0);
;   od = __builtin_amdgcn_mfma_f32_32x32x16_bf16(pa3, ATT_PK(vf[6], vf[7]), od, 0, 0, 0);
;     ...
; }
; template <int DV> __device__ __forceinline__ void pv_all_pipe(f32x16* o, int vb, bf16x8 pa0, bf16x8 pa1, bf16x8 pa2, bf16x8 pa3) {
;   s16x4 va[8], vc[8];
;   v_group_read<DV, 0>(va, vb); v_group_read<DV, 1>(vc, vb);
;   lgkm_wait8<8>(va); pv_group(o[0], va, pa0, pa1, pa2, pa3);
;   if constexpr (DV == 128) {
;     s16x4 vd[8], ve[8];
;     v_group_read<DV, 2>(vd, vb);
;     lgkm_wait8<8>(vc); pv_group(o[1], vc, pa0, pa1, pa2, pa3);
;     v_group_read<DV, 3>(ve, vb);
;     lgkm_wait8<8>(vd); pv_group(o[2], vd, pa0, pa1, pa2, pa3);
;     lgkm_wait8<0>(ve); pv_group(o[3], ve, pa0, pa1, pa2, pa3);
.LBB0_872:
	ds_read_b128 v[82:85], v162 offset:49152
	ds_read_b128 v[86:89], v162 offset:53248
	ds_read_b128 v[130:133], v164 offset:49152
	ds_read_b128 v[134:137], v164 offset:53248
	v_exp_f32_e32 v66, v66
	v_add_f32_e32 v180, 0, v173
	v_add_f32_e32 v180, v174, v180
	v_add_f32_e32 v180, v175, v180
	v_add_f32_e32 v180, v184, v180
	v_add_f32_e32 v180, v185, v180
	v_add_f32_e32 v180, v186, v180
	v_add_f32_e32 v180, v187, v180
	v_add_f32_e32 v180, v188, v180
	v_add_f32_e32 v180, v189, v180
	v_add_f32_e32 v180, v190, v180
	v_add_f32_e32 v180, v191, v180
	v_add_f32_e32 v180, v192, v180
	v_add_f32_e32 v180, v193, v180
	v_add_f32_e32 v180, v194, v180
	v_add_f32_e32 v180, v195, v180
	v_add_f32_e32 v180, v196, v180
	s_waitcnt lgkmcnt(0)
	v_mfma_f32_32x32x16_bf16 v[98:113], v[82:85], v[114:117], 0
	v_exp_f32_e32 v67, v67
	v_exp_f32_e32 v68, v68
	v_exp_f32_e32 v69, v69
	v_exp_f32_e32 v70, v70
	v_exp_f32_e32 v71, v71
	v_exp_f32_e32 v72, v72
	v_exp_f32_e32 v73, v73
	v_mfma_f32_32x32x16_bf16 v[82:97], v[86:89], v[114:117], 0
	v_exp_f32_e32 v74, v74
	v_exp_f32_e32 v75, v75
	v_exp_f32_e32 v76, v76
	v_exp_f32_e32 v77, v77
	v_exp_f32_e32 v78, v78
	v_exp_f32_e32 v79, v79
	v_exp_f32_e32 v80, v80
	v_mfma_f32_32x32x16_bf16 v[98:113], v[130:133], v[118:121], v[98:113]
	v_exp_f32_e32 v81, v81
	v_mfma_f32_32x32x16_bf16 v[82:97], v[134:137], v[118:121], v[82:97]
	ds_read_b128 v[130:133], v166 offset:49152
	ds_read_b128 v[134:137], v166 offset:53248
	v_add_f32_e32 v180, v66, v180
	v_add_f32_e32 v180, v67, v180
	v_add_f32_e32 v180, v68, v180
	v_add_f32_e32 v180, v69, v180
	v_add_f32_e32 v180, v70, v180
	v_add_f32_e32 v180, v71, v180
	v_add_f32_e32 v180, v72, v180
	v_add_f32_e32 v180, v73, v180
	s_waitcnt lgkmcnt(0)
	v_mfma_f32_32x32x16_bf16 v[98:113], v[130:133], v[122:125], v[98:113]
	v_mfma_f32_32x32x16_bf16 v[82:97], v[134:137], v[122:125], v[82:97]
	ds_read_b128 v[130:133], v168 offset:49152
	ds_read_b128 v[134:137], v168 offset:53248
	v_add_f32_e32 v180, v74, v180
	v_add_f32_e32 v180, v75, v180
	v_add_f32_e32 v180, v76, v180
	v_add_f32_e32 v180, v77, v180
	v_add_f32_e32 v180, v78, v180
	v_add_f32_e32 v180, v79, v180
	v_add_f32_e32 v180, v80, v180
	v_add_f32_e32 v180, v81, v180
	s_waitcnt lgkmcnt(0)
	v_mfma_f32_32x32x16_bf16 v[98:113], v[130:133], v[126:129], v[98:113]
	v_mfma_f32_32x32x16_bf16 v[82:97], v[134:137], v[126:129], v[82:97]
	v_add_f32_e32 v172, v172, v180
	v_cvt_pk_bf16_f32 v130, v173, v174
	v_cvt_pk_bf16_f32 v131, v175, v184
	v_cvt_pk_bf16_f32 v132, v185, v186
	v_cvt_pk_bf16_f32 v133, v187, v188
	v_cvt_pk_bf16_f32 v134, v189, v190
	v_cvt_pk_bf16_f32 v135, v191, v192
	v_cvt_pk_bf16_f32 v136, v193, v194
	v_cvt_pk_bf16_f32 v137, v195, v196
	v_cvt_pk_bf16_f32 v138, v66, v67
	v_cvt_pk_bf16_f32 v139, v68, v69
	v_cvt_pk_bf16_f32 v140, v70, v71
	v_cvt_pk_bf16_f32 v141, v72, v73
	v_cvt_pk_bf16_f32 v142, v74, v75
	v_cvt_pk_bf16_f32 v143, v76, v77
	v_cvt_pk_bf16_f32 v144, v78, v79
	v_cvt_pk_bf16_f32 v145, v80, v81
	ds_read_b64_tr_b16 v[176:177], v171 offset:0
	ds_read_b64_tr_b16 v[178:179], v171 offset:0x800
	ds_read_b64_tr_b16 v[198:199], v171 offset:0x1000
	ds_read_b64_tr_b16 v[200:201], v171 offset:0x1800
	ds_read_b64_tr_b16 v[202:203], v171 offset:0x2000
	ds_read_b64_tr_b16 v[204:205], v171 offset:0x2800
	ds_read_b64_tr_b16 v[206:207], v171 offset:0x3000
	ds_read_b64_tr_b16 v[208:209], v171 offset:0x3800
	ds_read_b64_tr_b16 v[210:211], v171 offset:0x200
	ds_read_b64_tr_b16 v[212:213], v171 offset:0xa00
	ds_read_b64_tr_b16 v[214:215], v171 offset:0x1200
	s_nop 0
	v_permlane32_swap_b32_e32 v130, v132
	v_permlane32_swap_b32_e32 v131, v133
	ds_read_b64_tr_b16 v[216:217], v171 offset:0x1a00
	ds_read_b64_tr_b16 v[218:219], v171 offset:0x2200
	ds_read_b64_tr_b16 v[220:221], v171 offset:0x2a00
	ds_read_b64_tr_b16 v[222:223], v171 offset:0x3200
	ds_read_b64_tr_b16 v[224:225], v171 offset:0x3a00
	s_waitcnt lgkmcnt(8)
	v_permlane32_swap_b32_e32 v134, v136
	s_nop 0
	v_mfma_f32_32x32x16_bf16 v[2:17], v[130:133], v[176:179], v[2:17]
	v_permlane32_swap_b32_e32 v135, v137
	v_permlane32_swap_b32_e32 v138, v140
	v_permlane32_swap_b32_e32 v139, v141
	ds_read_b64_tr_b16 v[176:177], v171 offset:0x400
	v_mfma_f32_32x32x16_bf16 v[2:17], v[134:137], v[198:201], v[2:17]
	v_permlane32_swap_b32_e32 v142, v144
	v_permlane32_swap_b32_e32 v143, v145
	ds_read_b64_tr_b16 v[178:179], v171 offset:0xc00
	ds_read_b64_tr_b16 v[198:199], v171 offset:0x1400
	ds_read_b64_tr_b16 v[200:201], v171 offset:0x1c00
	v_mfma_f32_32x32x16_bf16 v[2:17], v[138:141], v[202:205], v[2:17]
	ds_read_b64_tr_b16 v[202:203], v171 offset:0x2400
	ds_read_b64_tr_b16 v[204:205], v171 offset:0x2c00
	v_exp_f32_e32 v197, v98
	v_mfma_f32_32x32x16_bf16 v[2:17], v[142:145], v[206:209], v[2:17]
	ds_read_b64_tr_b16 v[206:207], v171 offset:0x3400
	ds_read_b64_tr_b16 v[208:209], v171 offset:0x3c00
	s_waitcnt lgkmcnt(8)
	s_nop 0
	v_mfma_f32_32x32x16_bf16 v[50:65], v[130:133], v[210:213], v[50:65]
	ds_read_b64_tr_b16 v[210:211], v171 offset:0x600
	ds_read_b64_tr_b16 v[212:213], v171 offset:0xe00
	v_mfma_f32_32x32x16_bf16 v[50:65], v[134:137], v[214:217], v[50:65]
	ds_read_b64_tr_b16 v[214:215], v171 offset:0x1600
	ds_read_b64_tr_b16 v[216:217], v171 offset:0x1e00
	v_mfma_f32_32x32x16_bf16 v[50:65], v[138:141], v[218:221], v[50:65]
	ds_read_b64_tr_b16 v[218:219], v171 offset:0x2600
	ds_read_b64_tr_b16 v[220:221], v171 offset:0x2e00
	v_mfma_f32_32x32x16_bf16 v[50:65], v[142:145], v[222:225], v[50:65]
	ds_read_b64_tr_b16 v[222:223], v171 offset:0x3600
	ds_read_b64_tr_b16 v[224:225], v171 offset:0x3e00
	s_waitcnt lgkmcnt(8)
	s_nop 0
	s_waitcnt lgkmcnt(0)
	v_mfma_f32_32x32x16_bf16 v[34:49], v[130:133], v[176:179], v[34:49]
	v_mfma_f32_32x32x16_bf16 v[18:33], v[130:133], v[210:213], v[18:33]
	v_exp_f32_e32 v210, v105
	v_exp_f32_e32 v211, v111
	v_exp_f32_e32 v212, v113
	v_mfma_f32_32x32x16_bf16 v[34:49], v[134:137], v[198:201], v[34:49]
	v_exp_f32_e32 v200, v99
	v_exp_f32_e32 v198, v100
	v_exp_f32_e32 v199, v106
	v_exp_f32_e32 v201, v108
	v_mfma_f32_32x32x16_bf16 v[18:33], v[134:137], v[214:217], v[18:33]
	v_mfma_f32_32x32x16_bf16 v[34:49], v[138:141], v[202:205], v[34:49]
	v_exp_f32_e32 v202, v101
	v_exp_f32_e32 v204, v102
	v_exp_f32_e32 v205, v104
	v_exp_f32_e32 v203, v107
	v_mfma_f32_32x32x16_bf16 v[18:33], v[138:141], v[218:221], v[18:33]
	v_mfma_f32_32x32x16_bf16 v[34:49], v[142:145], v[206:209], v[34:49]
	v_exp_f32_e32 v207, v103
	v_exp_f32_e32 v209, v109
	v_exp_f32_e32 v206, v110
	v_exp_f32_e32 v208, v112
	v_mfma_f32_32x32x16_bf16 v[18:33], v[142:145], v[222:225], v[18:33]
	s_cmp_ge_u32 s57, s97
	s_cbranch_scc1 .LBB0_880

; #define DMA_WAIT(last) do { if (last) asm volatile("s_waitcnt vmcnt(0)" ::: "memory"); else asm volatile("s_waitcnt vmcnt(%0)" :: "n"(NPW) : "memory"); } while (0)
; template <int DK, int DV, bool OFF, class QLoader> ...
;     ...
;   f32x16 pA0, pA1, pB0, pB1; bf16x8 pa0, pa1, pa2, pa3; const int NT = nkeys / KVBLK;
;   DMA_TILE(0, 0); DMA_TILE(1, 1); DMA_WAIT(false); __syncthreads(); if (2 < NT) DMA_TILE(2, 2);
;   qkt<DK>(pA0, pA1, K_lds, qr, r32, hi); partialSM<DK, OFF>(pA0, pA1, negMC);
.LBB0_875:
.LBB0_877:
	s_cmp_ge_u32 s55, s95
	s_waitcnt vmcnt(0)
	s_barrier
	s_cbranch_scc1 .LBB0_879
	v_lshl_add_u64 v[66:67], v[156:157], 0, s[8:9]
	s_mov_b64 s[24:25], 0x1ec0c000
	s_mov_b32 m0, s89
	v_lshl_add_u64 v[66:67], v[66:67], 0, s[24:25]
	global_load_lds_dwordx4 v[66:67], off
	s_mov_b64 s[24:25], 0xdcc1000
	v_lshl_add_u64 v[66:67], v[152:153], 0, s[8:9]
	v_lshl_add_u64 v[68:69], v[66:67], 0, s[24:25]
	s_mov_b32 m0, s91
	s_mov_b64 s[24:25], 0xdcc1080
	global_load_lds_dwordx4 v[68:69], off
	v_lshl_add_u64 v[66:67], v[66:67], 0, s[24:25]
	s_mov_b32 m0, s92
	s_nop 0
	global_load_lds_dwordx4 v[66:67], off
; __device__ __forceinline__ void finishSM(f32x16& p0, f32x16& p1, float& l_reg, bf16x8& pa0, bf16x8& pa1, bf16x8& pa2, bf16x8& pa3) {
; #pragma unroll
;   for (int r = 0; r < 16; ++r) p1[r] = __builtin_amdgcn_exp2f(p1[r]);
;   float ps = 0;
; #pragma unroll
;   for (int r = 0; r < 16; ++r) ps += p0[r];
; #pragma unroll
;   for (int r = 0; r < 16; ++r) ps += p1[r];
;   l_reg += ps;
;     ...
;   ATT_PK4(p0, 0, pa0); ATT_PK4(p0, 8, pa1); ATT_PK4(p1, 0, pa2); ATT_PK4(p1, 8, pa3);
;     ...
; }
; template <int DK>
; __device__ __forceinline__ void qkt(f32x16& p0, f32x16& p1, const char* Ks, const bf16x8* qr, int r32, int hi) {
;   p0 = f32x16{}; p1 = f32x16{};
; #pragma unroll
;   for (int d0 = 0; d0 < DK / 16; ++d0) { const int cb = (d0 * 16 + hi * 8) * 2;
;     const bf16x8 b0 = *reinterpret_cast<const bf16x8*>(Ks + ATT_KSWZ(r32, cb));
;     const bf16x8 b1 = *reinterpret_cast<const bf16x8*>(Ks + ATT_KSWZ(32 + r32, cb));
;     p0 = __builtin_amdgcn_mfma_f32_32x32x16_bf16(b0, qr[d0], p0, 0, 0, 0);
;     p1 = __builtin_amdgcn_mfma_f32_32x32x16_bf16(b1, qr[d0], p1, 0, 0, 0);
;   }
; }
; template <int DV, int GRP> __device__ __forceinline__ void v_group_read(s16x4* vf, int vb) {
;   sfor<0, 8>([&](auto ic) { constexpr int j = decltype(ic)::value; vf[j] = tr_read<v_rd_off<DV>(GRP, j / 2, j % 2)>(vb); });
; }
; __device__ __forceinline__ void pv_group(f32x16& od, const s16x4* vf, bf16x8 pa0, bf16x8 pa1, bf16x8 pa2, bf16x8 pa3) {
;     ...
;   od = __builtin_amdgcn_mfma_f32_32x32x16_bf16(pa0, ATT_PK(vf[0], vf[1]), od, 0, 0, 0);
;   od = __builtin_amdgcn_mfma_f32_32x32x16_bf16(pa1, ATT_PK(vf[2], vf[3]), od, 0, 0, 0);
;   od = __builtin_amdgcn_mfma_f32_32x32x16_bf16(pa2, ATT_PK(vf[4], vf[5]), od, 0, 0, 0);
;   od = __builtin_amdgcn_mfma_f32_32x32x16_bf16(pa3, ATT_PK(vf[6], vf[7]), od, 0, 0, 0);
;     ...
; }
; template <int DV> __device__ __forceinline__ void pv_all_pipe(f32x16* o, int vb, bf16x8 pa0, bf16x8 pa1, bf16x8 pa2, bf16x8 pa3) {
;   s16x4 va[8], vc[8];
;   v_group_read<DV, 0>(va, vb); v_group_read<DV, 1>(vc, vb);
;   lgkm_wait8<8>(va); pv_group(o[0], va, pa0, pa1, pa2, pa3);
;   if constexpr (DV == 128) {
;     s16x4 vd[8], ve[8];
;     v_group_read<DV, 2>(vd, vb);
;     lgkm_wait8<8>(vc); pv_group(o[1], vc, pa0, pa1, pa2, pa3);
;     v_group_read<DV, 3>(ve, vb);
;     lgkm_wait8<8>(vd); pv_group(o[2], vd, pa0, pa1, pa2, pa3);
;     lgkm_wait8<0>(ve); pv_group(o[3], ve, pa0, pa1, pa2, pa3);
.LBB0_879:
	ds_read_b128 v[66:69], v162
	ds_read_b128 v[70:73], v162 offset:4096
	ds_read_b128 v[130:133], v164
	ds_read_b128 v[134:137], v164 offset:4096
	v_exp_f32_e32 v82, v82
	v_exp_f32_e32 v83, v83
	v_add_f32_e32 v180, 0, v197
	v_add_f32_e32 v180, v200, v180
	v_add_f32_e32 v180, v198, v180
	v_add_f32_e32 v180, v202, v180
	v_add_f32_e32 v180, v204, v180
	v_add_f32_e32 v180, v207, v180
	v_add_f32_e32 v180, v205, v180
	v_add_f32_e32 v180, v210, v180
	v_add_f32_e32 v180, v199, v180
	v_add_f32_e32 v180, v203, v180
	v_add_f32_e32 v180, v201, v180
	v_add_f32_e32 v180, v209, v180
	v_add_f32_e32 v180, v206, v180
	v_add_f32_e32 v180, v211, v180
	v_add_f32_e32 v180, v208, v180
	v_add_f32_e32 v180, v212, v180
	s_waitcnt lgkmcnt(0)
	v_mfma_f32_32x32x16_bf16 v[98:113], v[66:69], v[114:117], 0
	v_exp_f32_e32 v84, v84
	v_exp_f32_e32 v85, v85
	v_exp_f32_e32 v86, v86
	v_exp_f32_e32 v87, v87
	v_exp_f32_e32 v88, v88
	v_exp_f32_e32 v89, v89
	v_exp_f32_e32 v90, v90
	v_mfma_f32_32x32x16_bf16 v[66:81], v[70:73], v[114:117], 0
	v_exp_f32_e32 v91, v91
	v_exp_f32_e32 v92, v92
	v_exp_f32_e32 v93, v93
	v_exp_f32_e32 v94, v94
	v_exp_f32_e32 v95, v95
	v_exp_f32_e32 v96, v96
	v_exp_f32_e32 v97, v97
	v_mfma_f32_32x32x16_bf16 v[98:113], v[130:133], v[118:121], v[98:113]
	v_mfma_f32_32x32x16_bf16 v[66:81], v[134:137], v[118:121], v[66:81]
	ds_read_b128 v[130:133], v166
	ds_read_b128 v[134:137], v166 offset:4096
	v_add_f32_e32 v180, v82, v180
	v_add_f32_e32 v180, v83, v180
	v_add_f32_e32 v180, v84, v180
	v_add_f32_e32 v180, v85, v180
	v_add_f32_e32 v180, v86, v180
	v_add_f32_e32 v180, v87, v180
	v_add_f32_e32 v180, v88, v180
	v_add_f32_e32 v180, v89, v180
	s_waitcnt lgkmcnt(0)
	v_mfma_f32_32x32x16_bf16 v[98:113], v[130:133], v[122:125], v[98:113]
	v_mfma_f32_32x32x16_bf16 v[66:81], v[134:137], v[122:125], v[66:81]
	ds_read_b128 v[130:133], v168
	ds_read_b128 v[134:137], v168 offset:4096
	v_add_f32_e32 v180, v90, v180
	v_add_f32_e32 v180, v91, v180
	v_add_f32_e32 v180, v92, v180
	v_add_f32_e32 v180, v93, v180
	v_add_f32_e32 v180, v94, v180
	v_add_f32_e32 v180, v95, v180
	v_add_f32_e32 v180, v96, v180
	v_add_f32_e32 v180, v97, v180
	s_waitcnt lgkmcnt(0)
	v_mfma_f32_32x32x16_bf16 v[98:113], v[130:133], v[126:129], v[98:113]
	v_mfma_f32_32x32x16_bf16 v[66:81], v[134:137], v[126:129], v[66:81]
	v_add_f32_e32 v172, v172, v180
	v_cvt_pk_bf16_f32 v130, v197, v200
	v_cvt_pk_bf16_f32 v131, v198, v202
	v_cvt_pk_bf16_f32 v132, v204, v207
	v_cvt_pk_bf16_f32 v133, v205, v210
	v_cvt_pk_bf16_f32 v134, v199, v203
	v_cvt_pk_bf16_f32 v135, v201, v209
	v_cvt_pk_bf16_f32 v136, v206, v211
	v_cvt_pk_bf16_f32 v137, v208, v212
	v_cvt_pk_bf16_f32 v138, v82, v83
	v_cvt_pk_bf16_f32 v139, v84, v85
	v_cvt_pk_bf16_f32 v140, v86, v87
	v_cvt_pk_bf16_f32 v141, v88, v89
	v_cvt_pk_bf16_f32 v142, v90, v91
	v_cvt_pk_bf16_f32 v143, v92, v93
	v_cvt_pk_bf16_f32 v144, v94, v95
	v_cvt_pk_bf16_f32 v145, v96, v97
	ds_read_b64_tr_b16 v[174:175], v160 offset:0
	ds_read_b64_tr_b16 v[176:177], v160 offset:0x800
	ds_read_b64_tr_b16 v[184:185], v160 offset:0x1000
	ds_read_b64_tr_b16 v[186:187], v160 offset:0x1800
	ds_read_b64_tr_b16 v[188:189], v160 offset:0x2000
	ds_read_b64_tr_b16 v[190:191], v160 offset:0x2800
	ds_read_b64_tr_b16 v[192:193], v160 offset:0x3000
	ds_read_b64_tr_b16 v[194:195], v160 offset:0x3800
	ds_read_b64_tr_b16 v[214:215], v160 offset:0x200
	ds_read_b64_tr_b16 v[216:217], v160 offset:0xa00
	ds_read_b64_tr_b16 v[218:219], v160 offset:0x1200
	s_nop 0
	v_permlane32_swap_b32_e32 v130, v132
	v_permlane32_swap_b32_e32 v131, v133
	ds_read_b64_tr_b16 v[220:221], v160 offset:0x1a00
	ds_read_b64_tr_b16 v[222:223], v160 offset:0x2200
	ds_read_b64_tr_b16 v[224:225], v160 offset:0x2a00
	ds_read_b64_tr_b16 v[226:227], v160 offset:0x3200
	ds_read_b64_tr_b16 v[228:229], v160 offset:0x3a00
	s_waitcnt lgkmcnt(8)
	v_permlane32_swap_b32_e32 v134, v136
	s_nop 0
	v_mfma_f32_32x32x16_bf16 v[2:17], v[130:133], v[174:177], v[2:17]
	v_permlane32_swap_b32_e32 v135, v137
	v_permlane32_swap_b32_e32 v138, v140
	v_permlane32_swap_b32_e32 v139, v141
	ds_read_b64_tr_b16 v[174:175], v160 offset:0x400
	v_mfma_f32_32x32x16_bf16 v[2:17], v[134:137], v[184:187], v[2:17]
	v_permlane32_swap_b32_e32 v142, v144
	v_permlane32_swap_b32_e32 v143, v145
	ds_read_b64_tr_b16 v[176:177], v160 offset:0xc00
	ds_read_b64_tr_b16 v[184:185], v160 offset:0x1400
	ds_read_b64_tr_b16 v[186:187], v160 offset:0x1c00
	v_mfma_f32_32x32x16_bf16 v[2:17], v[138:141], v[188:191], v[2:17]
	ds_read_b64_tr_b16 v[188:189], v160 offset:0x2400
	ds_read_b64_tr_b16 v[190:191], v160 offset:0x2c00
	v_exp_f32_e32 v173, v98
	v_exp_f32_e32 v196, v113
	v_mfma_f32_32x32x16_bf16 v[2:17], v[142:145], v[192:195], v[2:17]
	ds_read_b64_tr_b16 v[192:193], v160 offset:0x3400
	ds_read_b64_tr_b16 v[194:195], v160 offset:0x3c00
	s_waitcnt lgkmcnt(8)
	s_nop 0
	v_mfma_f32_32x32x16_bf16 v[50:65], v[130:133], v[214:217], v[50:65]
	ds_read_b64_tr_b16 v[214:215], v160 offset:0x600
	ds_read_b64_tr_b16 v[216:217], v160 offset:0xe00
	v_mfma_f32_32x32x16_bf16 v[50:65], v[134:137], v[218:221], v[50:65]
	ds_read_b64_tr_b16 v[218:219], v160 offset:0x1600
	ds_read_b64_tr_b16 v[220:221], v160 offset:0x1e00
	v_mfma_f32_32x32x16_bf16 v[50:65], v[138:141], v[222:225], v[50:65]
	ds_read_b64_tr_b16 v[222:223], v160 offset:0x2600
	ds_read_b64_tr_b16 v[224:225], v160 offset:0x2e00
	v_mfma_f32_32x32x16_bf16 v[50:65], v[142:145], v[226:229], v[50:65]
	ds_read_b64_tr_b16 v[226:227], v160 offset:0x3600
	ds_read_b64_tr_b16 v[228:229], v160 offset:0x3e00
	s_waitcnt lgkmcnt(8)
	s_nop 0
	s_waitcnt lgkmcnt(0)
	v_mfma_f32_32x32x16_bf16 v[34:49], v[130:133], v[174:177], v[34:49]
	v_exp_f32_e32 v174, v99
	v_exp_f32_e32 v175, v100
	v_mfma_f32_32x32x16_bf16 v[18:33], v[130:133], v[214:217], v[18:33]
	v_mfma_f32_32x32x16_bf16 v[34:49], v[134:137], v[184:187], v[34:49]
	v_exp_f32_e32 v184, v101
	v_exp_f32_e32 v185, v102
	v_exp_f32_e32 v186, v103
	v_exp_f32_e32 v187, v104
	v_mfma_f32_32x32x16_bf16 v[18:33], v[134:137], v[218:221], v[18:33]
	v_mfma_f32_32x32x16_bf16 v[34:49], v[138:141], v[188:191], v[34:49]
	v_exp_f32_e32 v188, v105
	v_exp_f32_e32 v189, v106
	v_exp_f32_e32 v190, v107
	v_exp_f32_e32 v191, v108
	v_mfma_f32_32x32x16_bf16 v[18:33], v[138:141], v[222:225], v[18:33]
	v_mfma_f32_32x32x16_bf16 v[34:49], v[142:145], v[192:195], v[34:49]
	v_exp_f32_e32 v192, v109
	v_exp_f32_e32 v193, v110
	v_exp_f32_e32 v194, v111
	v_exp_f32_e32 v195, v112
	v_mfma_f32_32x32x16_bf16 v[18:33], v[142:145], v[226:229], v[18:33]
